# grid barrier: acquire invalidate issued when the workgroup has arrived (all its loads done, only sc1 polls follow) instead of after the release is observed; leaders invalidate after their L2 writeback
# speedup vs baseline: 1.0162x; 1.0075x over previous
.LBB0_78:
	s_or_b64 exec, exec, s[8:9]
	v_cvt_f32_u32_e32 v4, v2
	s_waitcnt vmcnt(0)
	v_readfirstlane_b32 s6, v3
	v_sub_u32_e32 v3, 0, v2
	v_rcp_iflag_f32_e32 v4, v4
	v_add_u32_e32 v5, s6, v1
	v_mul_f32_e32 v4, 0x4f7ffffe, v4
	v_cvt_u32_f32_e32 v4, v4
	v_mul_lo_u32 v1, v3, v4
	v_mul_hi_u32 v1, v4, v1
	v_add_u32_e32 v1, v4, v1
	v_mul_hi_u32 v1, v5, v1
	v_mul_lo_u32 v3, v1, v2
	v_sub_u32_e32 v3, v5, v3
	v_add_u32_e32 v4, 1, v1
	v_cmp_ge_u32_e32 vcc, v3, v2
	s_nop 1
	v_cndmask_b32_e32 v1, v1, v4, vcc
	v_sub_u32_e32 v4, v3, v2
	v_cndmask_b32_e32 v3, v3, v4, vcc
	v_add_u32_e32 v4, 1, v1
	v_cmp_ge_u32_e32 vcc, v3, v2
	v_add_u32_e32 v3, 1, v5
	s_nop 0
	v_cndmask_b32_e32 v1, v1, v4, vcc
	v_mul_lo_u32 v4, v2, v1
	v_add_u32_e32 v2, v4, v2
	v_cmp_ne_u32_e32 vcc, v3, v2
	s_and_saveexec_b64 s[6:7], vcc
	s_xor_b64 s[6:7], exec, s[6:7]
	s_cbranch_execz .LBB0_92
	s_waitcnt lgkmcnt(0)
	buffer_inv sc1
	v_mov_b32_e32 v0, 0x2000
	global_load_dword v0, v0, s[4:5] offset:1024 sc1
	s_add_u32 s12, s4, 0x2400
	s_addc_u32 s13, s5, 0
	s_waitcnt vmcnt(0)
	v_cmp_eq_u32_e32 vcc, v0, v1
	s_and_saveexec_b64 s[8:9], vcc
	s_cbranch_execz .LBB0_91
	s_add_u32 s10, s88, 0x80200
	s_addc_u32 s11, s89, 0
	s_mov_b32 s24, 1
	s_mov_b64 s[14:15], 0
	v_mov_b32_e32 v0, 0
	s_branch .LBB0_82

.LBB0_91:
	s_or_b64 exec, exec, s[8:9]
	s_waitcnt vmcnt(0)
	s_waitcnt vmcnt(0)

.LBB0_95:
	s_or_b64 exec, exec, s[8:9]
	v_cvt_f32_u32_e32 v3, v0
	s_waitcnt vmcnt(0)
	v_readfirstlane_b32 s6, v2
	s_add_u32 s8, s4, 0x2400
	s_addc_u32 s9, s5, 0
	v_rcp_iflag_f32_e32 v3, v3
	v_add_u32_e32 v1, s6, v1
	v_add_u32_e32 v4, 1, v1
	s_mov_b64 s[10:11], -1
	v_mul_f32_e32 v2, 0x4f7ffffe, v3
	v_cvt_u32_f32_e32 v2, v2
	v_sub_u32_e32 v3, 0, v0
	v_mul_lo_u32 v3, v3, v2
	v_mul_hi_u32 v3, v2, v3
	v_add_u32_e32 v2, v2, v3
	v_mul_hi_u32 v2, v1, v2
	v_mul_lo_u32 v3, v2, v0
	v_sub_u32_e32 v1, v1, v3
	v_add_u32_e32 v5, 1, v2
	v_cmp_ge_u32_e32 vcc, v1, v0
	v_sub_u32_e32 v3, v1, v0
	s_nop 0
	v_cndmask_b32_e32 v2, v2, v5, vcc
	v_cndmask_b32_e32 v1, v1, v3, vcc
	v_add_u32_e32 v3, 1, v2
	v_cmp_ge_u32_e32 vcc, v1, v0
	s_nop 1
	v_cndmask_b32_e32 v2, v2, v3, vcc
	v_mul_lo_u32 v1, v0, v2
	v_add_u32_e32 v0, v1, v0
	v_cmp_ne_u32_e32 vcc, v4, v0
	v_mov_b64_e32 v[0:1], s[8:9]
	s_and_saveexec_b64 s[6:7], vcc
	s_cbranch_execz .Lxbrel_0
	buffer_inv sc1
	v_mov_b32_e32 v0, 0
	global_load_dword v1, v0, s[8:9] sc1
	s_mov_b64 s[14:15], 0
	s_waitcnt vmcnt(0)
	v_cmp_eq_u32_e32 vcc, v1, v2
	s_and_saveexec_b64 s[12:13], vcc
	s_cbranch_execz .LBB0_106
	s_add_u32 s10, s88, 0x80200
	s_addc_u32 s11, s89, 0
	s_mov_b32 s24, 1
	s_branch .LBB0_99

.Lxbrel_0:
	s_mov_b64 exec, s[6:7]
	s_mov_b64 s[10:11], 0
	v_mov_b32_e32 v2, 1
	v_mov_b32_e32 v3, 0x82400
	global_atomic_add v3, v2, s[88:89]
	global_atomic_add v3, v2, s[88:89] offset:256
	global_atomic_add v3, v2, s[88:89] offset:512
	global_atomic_add v3, v2, s[88:89] offset:768
	global_atomic_add v3, v2, s[88:89] offset:1024
	global_atomic_add v3, v2, s[88:89] offset:1280
	global_atomic_add v3, v2, s[88:89] offset:1536
	global_atomic_add v3, v2, s[88:89] offset:1792
	global_atomic_add v3, v2, s[88:89] offset:2048
	global_atomic_add v3, v2, s[88:89] offset:2304
	global_atomic_add v3, v2, s[88:89] offset:2560
	global_atomic_add v3, v2, s[88:89] offset:2816
	global_atomic_add v3, v2, s[88:89] offset:3072
	global_atomic_add v3, v2, s[88:89] offset:3328
	global_atomic_add v3, v2, s[88:89] offset:3584
	global_atomic_add v3, v2, s[88:89] offset:3840
	buffer_inv sc1

.LBB0_109:
	s_or_b64 exec, exec, s[6:7]
	s_mov_b64 s[6:7], exec
	v_mbcnt_lo_u32_b32 v0, s6, 0
	v_mbcnt_hi_u32_b32 v0, s7, v0
	v_cmp_eq_u32_e32 vcc, 0, v0
	s_waitcnt vmcnt(0)
	s_and_saveexec_b64 s[8:9], vcc
	s_cbranch_execz .LBB0_111
	s_bcnt1_i32_b64 s6, s[6:7]
	v_mov_b32_e32 v0, 0x2000
	v_mov_b32_e32 v1, s6

.LBB0_149:
	s_or_b64 exec, exec, s[10:11]
	v_cvt_f32_u32_e32 v4, v2
	s_waitcnt vmcnt(0)
	v_readfirstlane_b32 s8, v3
	v_sub_u32_e32 v3, 0, v2
	v_rcp_iflag_f32_e32 v4, v4
	v_add_u32_e32 v5, s8, v1
	v_mul_f32_e32 v4, 0x4f7ffffe, v4
	v_cvt_u32_f32_e32 v4, v4
	v_mul_lo_u32 v1, v3, v4
	v_mul_hi_u32 v1, v4, v1
	v_add_u32_e32 v1, v4, v1
	v_mul_hi_u32 v1, v5, v1
	v_mul_lo_u32 v3, v1, v2
	v_sub_u32_e32 v3, v5, v3
	v_add_u32_e32 v4, 1, v1
	v_cmp_ge_u32_e32 vcc, v3, v2
	s_nop 1
	v_cndmask_b32_e32 v1, v1, v4, vcc
	v_sub_u32_e32 v4, v3, v2
	v_cndmask_b32_e32 v3, v3, v4, vcc
	v_add_u32_e32 v4, 1, v1
	v_cmp_ge_u32_e32 vcc, v3, v2
	v_add_u32_e32 v3, 1, v5
	s_nop 0
	v_cndmask_b32_e32 v1, v1, v4, vcc
	v_mul_lo_u32 v4, v2, v1
	v_add_u32_e32 v2, v4, v2
	v_cmp_ne_u32_e32 vcc, v3, v2
	s_and_saveexec_b64 s[8:9], vcc
	s_xor_b64 s[8:9], exec, s[8:9]
	s_cbranch_execz .LBB0_163
	s_waitcnt lgkmcnt(0)
	buffer_inv sc1
	v_mov_b32_e32 v0, 0x2000
	global_load_dword v0, v0, s[6:7] offset:1024 sc1
	s_add_u32 s14, s6, 0x2400
	s_addc_u32 s15, s7, 0
	s_waitcnt vmcnt(0)
	v_cmp_eq_u32_e32 vcc, v0, v1
	s_and_saveexec_b64 s[10:11], vcc
	s_cbranch_execz .LBB0_162
	s_add_u32 s12, s88, 0x80200
	s_addc_u32 s13, s89, 0
	s_mov_b32 s26, 1
	s_mov_b64 s[16:17], 0
	v_mov_b32_e32 v0, 0
	s_branch .LBB0_153

.LBB0_162:
	s_or_b64 exec, exec, s[10:11]
	s_waitcnt vmcnt(0)
	s_waitcnt vmcnt(0)

.LBB0_166:
	s_or_b64 exec, exec, s[10:11]
	v_cvt_f32_u32_e32 v3, v0
	s_waitcnt vmcnt(0)
	v_readfirstlane_b32 s8, v2
	s_add_u32 s10, s6, 0x2400
	s_addc_u32 s11, s7, 0
	v_rcp_iflag_f32_e32 v3, v3
	v_add_u32_e32 v1, s8, v1
	v_add_u32_e32 v4, 1, v1
	s_mov_b64 s[12:13], -1
	v_mul_f32_e32 v2, 0x4f7ffffe, v3
	v_cvt_u32_f32_e32 v2, v2
	v_sub_u32_e32 v3, 0, v0
	v_mul_lo_u32 v3, v3, v2
	v_mul_hi_u32 v3, v2, v3
	v_add_u32_e32 v2, v2, v3
	v_mul_hi_u32 v2, v1, v2
	v_mul_lo_u32 v3, v2, v0
	v_sub_u32_e32 v1, v1, v3
	v_add_u32_e32 v5, 1, v2
	v_cmp_ge_u32_e32 vcc, v1, v0
	v_sub_u32_e32 v3, v1, v0
	s_nop 0
	v_cndmask_b32_e32 v2, v2, v5, vcc
	v_cndmask_b32_e32 v1, v1, v3, vcc
	v_add_u32_e32 v3, 1, v2
	v_cmp_ge_u32_e32 vcc, v1, v0
	s_nop 1
	v_cndmask_b32_e32 v2, v2, v3, vcc
	v_mul_lo_u32 v1, v0, v2
	v_add_u32_e32 v0, v1, v0
	v_cmp_ne_u32_e32 vcc, v4, v0
	v_mov_b64_e32 v[0:1], s[10:11]
	s_and_saveexec_b64 s[8:9], vcc
	s_cbranch_execz .Lxbrel_1
	buffer_inv sc1
	v_mov_b32_e32 v0, 0
	global_load_dword v1, v0, s[10:11] sc1
	s_mov_b64 s[16:17], 0
	s_waitcnt vmcnt(0)
	v_cmp_eq_u32_e32 vcc, v1, v2
	s_and_saveexec_b64 s[14:15], vcc
	s_cbranch_execz .LBB0_177
	s_add_u32 s12, s88, 0x80200
	s_addc_u32 s13, s89, 0
	s_mov_b32 s26, 1
	s_branch .LBB0_170

.Lxbrel_1:
	s_mov_b64 exec, s[8:9]
	s_mov_b64 s[12:13], 0
	v_mov_b32_e32 v2, 1
	v_mov_b32_e32 v3, 0x82400
	global_atomic_add v3, v2, s[88:89]
	global_atomic_add v3, v2, s[88:89] offset:256
	global_atomic_add v3, v2, s[88:89] offset:512
	global_atomic_add v3, v2, s[88:89] offset:768
	global_atomic_add v3, v2, s[88:89] offset:1024
	global_atomic_add v3, v2, s[88:89] offset:1280
	global_atomic_add v3, v2, s[88:89] offset:1536
	global_atomic_add v3, v2, s[88:89] offset:1792
	global_atomic_add v3, v2, s[88:89] offset:2048
	global_atomic_add v3, v2, s[88:89] offset:2304
	global_atomic_add v3, v2, s[88:89] offset:2560
	global_atomic_add v3, v2, s[88:89] offset:2816
	global_atomic_add v3, v2, s[88:89] offset:3072
	global_atomic_add v3, v2, s[88:89] offset:3328
	global_atomic_add v3, v2, s[88:89] offset:3584
	global_atomic_add v3, v2, s[88:89] offset:3840
	buffer_inv sc1

.LBB0_180:
	s_or_b64 exec, exec, s[8:9]
	s_mov_b64 s[8:9], exec
	v_mbcnt_lo_u32_b32 v0, s8, 0
	v_mbcnt_hi_u32_b32 v0, s9, v0
	v_cmp_eq_u32_e32 vcc, 0, v0
	s_waitcnt vmcnt(0)
	s_and_saveexec_b64 s[10:11], vcc
	s_cbranch_execz .LBB0_182
	s_bcnt1_i32_b64 s8, s[8:9]
	v_mov_b32_e32 v0, 0x2000
	v_mov_b32_e32 v1, s8

.LBB0_617:
	s_or_b64 exec, exec, s[8:9]
	v_cvt_f32_u32_e32 v4, v2
	s_waitcnt vmcnt(0)
	v_readfirstlane_b32 s6, v3
	v_sub_u32_e32 v3, 0, v2
	v_rcp_iflag_f32_e32 v4, v4
	v_add_u32_e32 v5, s6, v1
	v_mul_f32_e32 v4, 0x4f7ffffe, v4
	v_cvt_u32_f32_e32 v4, v4
	v_mul_lo_u32 v1, v3, v4
	v_mul_hi_u32 v1, v4, v1
	v_add_u32_e32 v1, v4, v1
	v_mul_hi_u32 v1, v5, v1
	v_mul_lo_u32 v3, v1, v2
	v_sub_u32_e32 v3, v5, v3
	v_add_u32_e32 v4, 1, v1
	v_cmp_ge_u32_e32 vcc, v3, v2
	s_nop 1
	v_cndmask_b32_e32 v1, v1, v4, vcc
	v_sub_u32_e32 v4, v3, v2
	v_cndmask_b32_e32 v3, v3, v4, vcc
	v_add_u32_e32 v4, 1, v1
	v_cmp_ge_u32_e32 vcc, v3, v2
	v_add_u32_e32 v3, 1, v5
	s_nop 0
	v_cndmask_b32_e32 v1, v1, v4, vcc
	v_mul_lo_u32 v4, v2, v1
	v_add_u32_e32 v2, v4, v2
	v_cmp_ne_u32_e32 vcc, v3, v2
	s_and_saveexec_b64 s[6:7], vcc
	s_xor_b64 s[6:7], exec, s[6:7]
	s_cbranch_execz .LBB0_631
	s_waitcnt lgkmcnt(0)
	buffer_inv sc1
	v_mov_b32_e32 v0, 0x2000
	global_load_dword v0, v0, s[4:5] offset:1024 sc1
	s_add_u32 s14, s4, 0x2400
	s_addc_u32 s15, s5, 0
	s_waitcnt vmcnt(0)
	v_cmp_eq_u32_e32 vcc, v0, v1
	s_and_saveexec_b64 s[8:9], vcc
	s_cbranch_execz .LBB0_630
	s_add_u32 s12, s88, 0x80200
	s_addc_u32 s13, s89, 0
	s_mov_b32 s26, 1
	s_mov_b64 s[16:17], 0
	v_mov_b32_e32 v0, 0
	s_branch .LBB0_621

.LBB0_634:
	s_or_b64 exec, exec, s[8:9]
	v_cvt_f32_u32_e32 v3, v0
	s_waitcnt vmcnt(0)
	v_readfirstlane_b32 s6, v2
	s_add_u32 s8, s4, 0x2400
	s_addc_u32 s9, s5, 0
	v_rcp_iflag_f32_e32 v3, v3
	v_add_u32_e32 v1, s6, v1
	v_add_u32_e32 v4, 1, v1
	s_mov_b64 s[12:13], -1
	v_mul_f32_e32 v2, 0x4f7ffffe, v3
	v_cvt_u32_f32_e32 v2, v2
	v_sub_u32_e32 v3, 0, v0
	v_mul_lo_u32 v3, v3, v2
	v_mul_hi_u32 v3, v2, v3
	v_add_u32_e32 v2, v2, v3
	v_mul_hi_u32 v2, v1, v2
	v_mul_lo_u32 v3, v2, v0
	v_sub_u32_e32 v1, v1, v3
	v_add_u32_e32 v5, 1, v2
	v_cmp_ge_u32_e32 vcc, v1, v0
	v_sub_u32_e32 v3, v1, v0
	s_nop 0
	v_cndmask_b32_e32 v2, v2, v5, vcc
	v_cndmask_b32_e32 v1, v1, v3, vcc
	v_add_u32_e32 v3, 1, v2
	v_cmp_ge_u32_e32 vcc, v1, v0
	s_nop 1
	v_cndmask_b32_e32 v2, v2, v3, vcc
	v_mul_lo_u32 v1, v0, v2
	v_add_u32_e32 v0, v1, v0
	v_cmp_ne_u32_e32 vcc, v4, v0
	v_mov_b64_e32 v[0:1], s[8:9]
	s_and_saveexec_b64 s[6:7], vcc
	s_cbranch_execz .Lxbrel_5
	buffer_inv sc1
	v_mov_b32_e32 v0, 0
	global_load_dword v1, v0, s[8:9] sc1
	s_mov_b64 s[16:17], 0
	s_waitcnt vmcnt(0)
	v_cmp_eq_u32_e32 vcc, v1, v2
	s_and_saveexec_b64 s[14:15], vcc
	s_cbranch_execz .LBB0_645
	s_add_u32 s12, s88, 0x80200
	s_addc_u32 s13, s89, 0
	s_mov_b32 s26, 1
	s_branch .LBB0_638

.Lxbrel_5:
	s_mov_b64 exec, s[6:7]
	s_mov_b64 s[12:13], 0
	v_mov_b32_e32 v2, 1
	v_mov_b32_e32 v3, 0x82400
	global_atomic_add v3, v2, s[88:89]
	global_atomic_add v3, v2, s[88:89] offset:256
	global_atomic_add v3, v2, s[88:89] offset:512
	global_atomic_add v3, v2, s[88:89] offset:768
	global_atomic_add v3, v2, s[88:89] offset:1024
	global_atomic_add v3, v2, s[88:89] offset:1280
	global_atomic_add v3, v2, s[88:89] offset:1536
	global_atomic_add v3, v2, s[88:89] offset:1792
	global_atomic_add v3, v2, s[88:89] offset:2048
	global_atomic_add v3, v2, s[88:89] offset:2304
	global_atomic_add v3, v2, s[88:89] offset:2560
	global_atomic_add v3, v2, s[88:89] offset:2816
	global_atomic_add v3, v2, s[88:89] offset:3072
	global_atomic_add v3, v2, s[88:89] offset:3328
	global_atomic_add v3, v2, s[88:89] offset:3584
	global_atomic_add v3, v2, s[88:89] offset:3840
	buffer_inv sc1

.LBB0_682:
	s_or_b64 exec, exec, s[8:9]
	v_cvt_f32_u32_e32 v4, v2
	s_waitcnt vmcnt(0)
	v_readfirstlane_b32 s6, v3
	v_sub_u32_e32 v3, 0, v2
	v_rcp_iflag_f32_e32 v4, v4
	v_add_u32_e32 v5, s6, v1
	v_mul_f32_e32 v4, 0x4f7ffffe, v4
	v_cvt_u32_f32_e32 v4, v4
	v_mul_lo_u32 v1, v3, v4
	v_mul_hi_u32 v1, v4, v1
	v_add_u32_e32 v1, v4, v1
	v_mul_hi_u32 v1, v5, v1
	v_mul_lo_u32 v3, v1, v2
	v_sub_u32_e32 v3, v5, v3
	v_add_u32_e32 v4, 1, v1
	v_cmp_ge_u32_e32 vcc, v3, v2
	s_nop 1
	v_cndmask_b32_e32 v1, v1, v4, vcc
	v_sub_u32_e32 v4, v3, v2
	v_cndmask_b32_e32 v3, v3, v4, vcc
	v_add_u32_e32 v4, 1, v1
	v_cmp_ge_u32_e32 vcc, v3, v2
	v_add_u32_e32 v3, 1, v5
	s_nop 0
	v_cndmask_b32_e32 v1, v1, v4, vcc
	v_mul_lo_u32 v4, v2, v1
	v_add_u32_e32 v2, v4, v2
	v_cmp_ne_u32_e32 vcc, v3, v2
	s_and_saveexec_b64 s[6:7], vcc
	s_xor_b64 s[6:7], exec, s[6:7]
	s_cbranch_execz .LBB0_696
	s_waitcnt lgkmcnt(0)
	buffer_inv sc1
	v_mov_b32_e32 v0, 0x2000
	global_load_dword v0, v0, s[4:5] offset:1024 sc1
	s_add_u32 s14, s4, 0x2400
	s_addc_u32 s15, s5, 0
	s_waitcnt vmcnt(0)
	v_cmp_eq_u32_e32 vcc, v0, v1
	s_and_saveexec_b64 s[8:9], vcc
	s_cbranch_execz .LBB0_695
	s_add_u32 s10, s88, 0x80200
	s_addc_u32 s11, s89, 0
	s_mov_b32 s26, 1
	s_mov_b64 s[16:17], 0
	v_mov_b32_e32 v0, 0
	s_branch .LBB0_686

.LBB0_699:
	s_or_b64 exec, exec, s[8:9]
	v_cvt_f32_u32_e32 v3, v0
	s_waitcnt vmcnt(0)
	v_readfirstlane_b32 s6, v2
	s_add_u32 s8, s4, 0x2400
	s_addc_u32 s9, s5, 0
	v_rcp_iflag_f32_e32 v3, v3
	v_add_u32_e32 v1, s6, v1
	v_add_u32_e32 v4, 1, v1
	s_mov_b64 s[10:11], -1
	v_mul_f32_e32 v2, 0x4f7ffffe, v3
	v_cvt_u32_f32_e32 v2, v2
	v_sub_u32_e32 v3, 0, v0
	v_mul_lo_u32 v3, v3, v2
	v_mul_hi_u32 v3, v2, v3
	v_add_u32_e32 v2, v2, v3
	v_mul_hi_u32 v2, v1, v2
	v_mul_lo_u32 v3, v2, v0
	v_sub_u32_e32 v1, v1, v3
	v_add_u32_e32 v5, 1, v2
	v_cmp_ge_u32_e32 vcc, v1, v0
	v_sub_u32_e32 v3, v1, v0
	s_nop 0
	v_cndmask_b32_e32 v2, v2, v5, vcc
	v_cndmask_b32_e32 v1, v1, v3, vcc
	v_add_u32_e32 v3, 1, v2
	v_cmp_ge_u32_e32 vcc, v1, v0
	s_nop 1
	v_cndmask_b32_e32 v2, v2, v3, vcc
	v_mul_lo_u32 v1, v0, v2
	v_add_u32_e32 v0, v1, v0
	v_cmp_ne_u32_e32 vcc, v4, v0
	v_mov_b64_e32 v[0:1], s[8:9]
	s_and_saveexec_b64 s[6:7], vcc
	s_cbranch_execz .Lxbrel_6
	buffer_inv sc1
	v_mov_b32_e32 v0, 0
	global_load_dword v1, v0, s[8:9] sc1
	s_mov_b64 s[16:17], 0
	s_waitcnt vmcnt(0)
	v_cmp_eq_u32_e32 vcc, v1, v2
	s_and_saveexec_b64 s[14:15], vcc
	s_cbranch_execz .LBB0_710
	s_add_u32 s10, s88, 0x80200
	s_addc_u32 s11, s89, 0
	s_mov_b32 s26, 1
	s_branch .LBB0_703

.LBB0_762:
	s_or_b64 exec, exec, s[10:11]
	v_cvt_f32_u32_e32 v4, v2
	s_waitcnt vmcnt(0)
	v_readfirstlane_b32 s8, v3
	v_sub_u32_e32 v3, 0, v2
	v_rcp_iflag_f32_e32 v4, v4
	v_add_u32_e32 v5, s8, v1
	v_mul_f32_e32 v4, 0x4f7ffffe, v4
	v_cvt_u32_f32_e32 v4, v4
	v_mul_lo_u32 v1, v3, v4
	v_mul_hi_u32 v1, v4, v1
	v_add_u32_e32 v1, v4, v1
	v_mul_hi_u32 v1, v5, v1
	v_mul_lo_u32 v3, v1, v2
	v_sub_u32_e32 v3, v5, v3
	v_add_u32_e32 v4, 1, v1
	v_cmp_ge_u32_e32 vcc, v3, v2
	s_nop 1
	v_cndmask_b32_e32 v1, v1, v4, vcc
	v_sub_u32_e32 v4, v3, v2
	v_cndmask_b32_e32 v3, v3, v4, vcc
	v_add_u32_e32 v4, 1, v1
	v_cmp_ge_u32_e32 vcc, v3, v2
	v_add_u32_e32 v3, 1, v5
	s_nop 0
	v_cndmask_b32_e32 v1, v1, v4, vcc
	v_mul_lo_u32 v4, v2, v1
	v_add_u32_e32 v2, v4, v2
	v_cmp_ne_u32_e32 vcc, v3, v2
	s_and_saveexec_b64 s[8:9], vcc
	s_xor_b64 s[8:9], exec, s[8:9]
	s_cbranch_execz .LBB0_776
	s_waitcnt lgkmcnt(0)
	buffer_inv sc1
	v_mov_b32_e32 v0, 0x2000
	global_load_dword v0, v0, s[4:5] offset:1024 sc1
	s_add_u32 s14, s4, 0x2400
	s_addc_u32 s15, s5, 0
	s_waitcnt vmcnt(0)
	v_cmp_eq_u32_e32 vcc, v0, v1
	s_and_saveexec_b64 s[10:11], vcc
	s_cbranch_execz .LBB0_775
	s_add_u32 s12, s88, 0x80200
	s_addc_u32 s13, s89, 0
	s_mov_b32 s26, 1
	s_mov_b64 s[16:17], 0
	v_mov_b32_e32 v0, 0
	s_branch .LBB0_766

.LBB0_779:
	s_or_b64 exec, exec, s[10:11]
	v_cvt_f32_u32_e32 v3, v0
	s_waitcnt vmcnt(0)
	v_readfirstlane_b32 s8, v2
	s_add_u32 s10, s4, 0x2400
	s_addc_u32 s11, s5, 0
	v_rcp_iflag_f32_e32 v3, v3
	v_add_u32_e32 v1, s8, v1
	v_add_u32_e32 v4, 1, v1
	s_mov_b64 s[12:13], -1
	v_mul_f32_e32 v2, 0x4f7ffffe, v3
	v_cvt_u32_f32_e32 v2, v2
	v_sub_u32_e32 v3, 0, v0
	v_mul_lo_u32 v3, v3, v2
	v_mul_hi_u32 v3, v2, v3
	v_add_u32_e32 v2, v2, v3
	v_mul_hi_u32 v2, v1, v2
	v_mul_lo_u32 v3, v2, v0
	v_sub_u32_e32 v1, v1, v3
	v_add_u32_e32 v5, 1, v2
	v_cmp_ge_u32_e32 vcc, v1, v0
	v_sub_u32_e32 v3, v1, v0
	s_nop 0
	v_cndmask_b32_e32 v2, v2, v5, vcc
	v_cndmask_b32_e32 v1, v1, v3, vcc
	v_add_u32_e32 v3, 1, v2
	v_cmp_ge_u32_e32 vcc, v1, v0
	s_nop 1
	v_cndmask_b32_e32 v2, v2, v3, vcc
	v_mul_lo_u32 v1, v0, v2
	v_add_u32_e32 v0, v1, v0
	v_cmp_ne_u32_e32 vcc, v4, v0
	v_mov_b64_e32 v[0:1], s[10:11]
	s_and_saveexec_b64 s[8:9], vcc
	s_cbranch_execz .Lxbrel_7
	buffer_inv sc1
	v_mov_b32_e32 v0, 0
	global_load_dword v1, v0, s[10:11] sc1
	s_mov_b64 s[16:17], 0
	s_waitcnt vmcnt(0)
	v_cmp_eq_u32_e32 vcc, v1, v2
	s_and_saveexec_b64 s[14:15], vcc
	s_cbranch_execz .LBB0_790
	s_add_u32 s12, s88, 0x80200
	s_addc_u32 s13, s89, 0
	s_mov_b32 s26, 1
	s_branch .LBB0_783
